# baseline (speedup 1.0000x reference)
_Z7k_protoPKfPf:
	s_load_dwordx4 s[4:7], s[0:1], 0x0
	v_and_b32_e32 v1, 15, v0
	v_lshrrev_b32_e32 v46, 4, v0
	s_lshl_b32 s0, s3, 11
	v_lshl_or_b32 v18, v46, 6, s0
	v_lshlrev_b32_e32 v42, 4, v1
	v_mov_b32_e32 v43, 0
	s_waitcnt lgkmcnt(0)
	v_lshl_add_u64 v[20:21], s[4:5], 0, v[42:43]
	v_ashrrev_i32_e32 v19, 31, v18
	s_mul_i32 s8, s2, 5
	v_lshl_add_u64 v[30:31], v[18:19], 2, v[20:21]
	v_mov_b32_e32 v43, 0x28000
	v_or_b32_e32 v18, 0x400, v18
	v_mad_i64_i32 v[10:11], s[0:1], s8, v43, v[30:31]
	s_add_i32 s4, s8, 1
	s_add_i32 s5, s8, 2
	v_ashrrev_i32_e32 v19, 31, v18
	v_mad_i64_i32 v[12:13], s[0:1], s4, v43, v[30:31]
	global_load_dwordx4 v[2:5], v[10:11], off nt
	global_load_dwordx4 v[6:9], v[12:13], off nt
	v_mad_i64_i32 v[22:23], s[0:1], s5, v43, v[30:31]
	s_add_i32 s9, s8, 3
	v_lshl_add_u64 v[38:39], v[18:19], 2, v[20:21]
	v_mad_i64_i32 v[24:25], s[0:1], s9, v43, v[30:31]
	global_load_dwordx4 v[10:13], v[22:23], off nt
	global_load_dwordx4 v[14:17], v[24:25], off nt
	v_mad_i64_i32 v[18:19], s[0:1], s8, v43, v[38:39]
	v_mad_i64_i32 v[22:23], s[0:1], s4, v43, v[38:39]
	s_add_i32 s10, s8, 4
	global_load_dwordx4 v[18:21], v[18:19], off nt
	v_mad_i64_i32 v[26:27], s[0:1], s5, v43, v[38:39]
	global_load_dwordx4 v[22:25], v[22:23], off nt
	v_mad_i64_i32 v[44:45], s[0:1], s9, v43, v[38:39]
	global_load_dwordx4 v[26:29], v[26:27], off nt
	v_mad_i64_i32 v[40:41], s[0:1], s10, v43, v[30:31]
	global_load_dwordx4 v[30:33], v[44:45], off nt
	global_load_dwordx4 v[34:37], v[40:41], off nt
	v_mad_i64_i32 v[38:39], s[0:1], s10, v43, v[38:39]
	global_load_dwordx4 v[38:41], v[38:39], off nt
	s_movk_i32 s1, 0x120
	s_mov_b32 s0, 0x3e4ccccd
	v_lshrrev_b32_e32 v43, 3, v0
	v_bfe_u32 v44, v0, 4, 2
	v_and_or_b32 v43, v43, 24, v44
	v_lshlrev_b32_e32 v43, 1, v43
	v_mad_u32_u24 v43, v1, s1, v43
	v_cmp_gt_u32_e32 vcc, 64, v0
	s_mul_i32 s4, s2, 20
	v_lshl_or_b32 v42, v46, 8, v42
	s_waitcnt vmcnt(8)
	v_pk_add_f32 v[2:3], v[2:3], v[6:7]
	v_pk_add_f32 v[4:5], v[4:5], v[8:9]
	s_waitcnt vmcnt(7)
	v_pk_add_f32 v[2:3], v[2:3], v[10:11]
	s_waitcnt vmcnt(6)
	v_pk_add_f32 v[2:3], v[2:3], v[14:15]
	v_pk_add_f32 v[4:5], v[4:5], v[12:13]
	s_waitcnt vmcnt(4)
	v_pk_add_f32 v[8:9], v[18:19], v[22:23]
	v_pk_add_f32 v[6:7], v[20:21], v[24:25]
	v_pk_add_f32 v[4:5], v[4:5], v[16:17]
	s_waitcnt vmcnt(3)
	v_pk_add_f32 v[8:9], v[8:9], v[26:27]
	v_pk_add_f32 v[6:7], v[6:7], v[28:29]
	s_waitcnt vmcnt(2)
	v_pk_add_f32 v[8:9], v[8:9], v[30:31]
	s_waitcnt vmcnt(1)
	v_pk_add_f32 v[2:3], v[2:3], v[34:35]
	v_pk_add_f32 v[6:7], v[6:7], v[32:33]
	v_pk_mul_f32 v[2:3], v[2:3], s[0:1] op_sel_hi:[1,0]
	s_waitcnt vmcnt(0)
	v_pk_add_f32 v[8:9], v[8:9], v[38:39]
	v_cvt_f16_f32_e32 v10, v2
	v_pk_add_f32 v[4:5], v[4:5], v[36:37]
	v_pk_add_f32 v[6:7], v[6:7], v[40:41]
	v_pk_mul_f32 v[8:9], v[8:9], s[0:1] op_sel_hi:[1,0]
	v_cvt_f16_f32_e32 v11, v3
	v_pk_mul_f32 v[4:5], v[4:5], s[0:1] op_sel_hi:[1,0]
	v_pk_mul_f32 v[6:7], v[6:7], s[0:1] op_sel_hi:[1,0]
	v_cvt_f16_f32_e32 v12, v8
	v_cvt_f16_f32_e32 v13, v9
	v_pk_mul_f32 v[8:9], v[8:9], v[8:9]
	v_cvt_f16_f32_e32 v14, v4
	v_cvt_f16_f32_e32 v16, v6
	v_cvt_f16_f32_e32 v17, v7
	v_pk_mul_f32 v[6:7], v[6:7], v[6:7]
	v_cvt_f16_f32_e32 v15, v5
	v_pk_fma_f32 v[2:3], v[2:3], v[2:3], v[8:9]
	v_pk_fma_f32 v[4:5], v[4:5], v[4:5], v[6:7]
	ds_write_b16 v43, v10
	ds_write_b16 v43, v11 offset:72
	ds_write_b16 v43, v12 offset:8
	ds_write_b16 v43, v14 offset:144
	ds_write_b16 v43, v15 offset:216
	ds_write_b16 v43, v17 offset:224
	ds_write_b16 v43, v13 offset:80
	ds_write_b16 v43, v16 offset:152
	ds_write_b128 v42, v[2:5] offset:4608
	s_waitcnt lgkmcnt(0)
	s_barrier
	s_mul_hi_i32 s1, s2, 20
	s_ashr_i32 s2, s3, 31
	v_lshrrev_b32_e32 v23, 2, v0
	s_add_u32 s0, s4, s3
	v_and_b32_e32 v23, 48, v23
	s_addc_u32 s1, s1, s2
	v_and_b32_e32 v22, 63, v0
	v_mul_u32_u24_e32 v23, 0x48, v23
	v_mul_u32_u24_e32 v21, 0x48, v1
	v_and_b32_e32 v24, 48, v0
	s_lshl_b64 s[0:1], s[0:1], 8
	v_and_b32_e32 v20, 0xc0, v0
	v_add3_u32 v23, v23, v21, v24
	v_or3_b32 v20, s0, v20, v22
	v_mov_b32_e32 v21, s1
	s_add_u32 s8, s6, 0x32000
	s_addc_u32 s9, s7, 0
	ds_read2_b64 v[26:29], v23 offset1:1
	v_lshl_add_u64 v[24:25], v[20:21], 4, s[8:9]
	s_waitcnt lgkmcnt(0)
	global_store_dwordx4 v[24:25], v[26:29], off
	s_and_saveexec_b64 s[0:1], vcc
	s_cbranch_execz .LBB0_2
	v_lshlrev_b32_e32 v12, 2, v0
	ds_read2st64_b32 v[2:3], v12 offset0:18 offset1:19
	ds_read2st64_b32 v[4:5], v12 offset0:20 offset1:21
	ds_read2st64_b32 v[6:7], v12 offset0:22 offset1:23
	ds_read2st64_b32 v[8:9], v12 offset0:24 offset1:25
	ds_read2st64_b32 v[10:11], v12 offset0:26 offset1:27
	ds_read2st64_b32 v[14:15], v12 offset0:28 offset1:29
	ds_read2st64_b32 v[16:17], v12 offset0:30 offset1:31
	ds_read2st64_b32 v[18:19], v12 offset0:32 offset1:33
	s_waitcnt lgkmcnt(7)
	v_add_f32_e32 v2, 0, v2
	v_add_f32_e32 v2, v2, v3
	s_waitcnt lgkmcnt(6)
	v_add_f32_e32 v2, v2, v4
	v_add_f32_e32 v2, v2, v5
	s_waitcnt lgkmcnt(5)
	v_add_f32_e32 v2, v2, v6
	v_add_f32_e32 v2, v2, v7
	s_waitcnt lgkmcnt(4)
	v_add_f32_e32 v2, v2, v8
	v_add_f32_e32 v2, v2, v9
	s_waitcnt lgkmcnt(3)
	v_add_f32_e32 v2, v2, v10
	v_add_f32_e32 v2, v2, v11
	s_waitcnt lgkmcnt(2)
	v_add_f32_e32 v2, v2, v14
	v_add_f32_e32 v2, v2, v15
	s_waitcnt lgkmcnt(1)
	v_add_f32_e32 v2, v2, v16
	v_add_f32_e32 v2, v2, v17
	s_waitcnt lgkmcnt(0)
	v_add_f32_e32 v2, v2, v18
	s_add_i32 s5, s4, s3
	v_add_f32_e32 v4, v2, v19
	v_lshl_or_b32 v2, s5, 6, v0
	v_ashrrev_i32_e32 v3, 31, v2
	v_lshl_add_u64 v[2:3], v[2:3], 2, s[6:7]
	global_store_dword v[2:3], v4, off
